# baseline (speedup 1.0000x reference)
.Lq_go_0:
	ds_read_b128 v[228:231], v5 offset:0
	ds_read_b128 v[232:235], v5 offset:512
	ds_read_b128 v[236:239], v5 offset:1024
	ds_read_b128 v[240:243], v5 offset:1536
	v_mul_f32_e32 v244, v84, v88
	v_mul_f32_e32 v250, v85, v89
	v_mul_f32_e64 v245, -v88, v88
	v_mul_f32_e64 v251, -v89, v89
	v_add_f32_e32 v246, v84, v88
	v_add_f32_e32 v252, v85, v89
	v_fma_f32 v245, -v84, v84, v245
	v_fma_f32 v251, -v85, v85, v251
	v_fma_f32 v247, v10, v246, v11
	v_fma_f32 v253, v10, v252, v11
	v_fma_f32 v246, v13, v96, v14
	v_fma_f32 v252, v13, v97, v14
	v_fma_f32 v248, v12, v92, v245
	v_fma_f32 v254, v12, v93, v251
	v_fma_f32 v249, 2.0, v244, v247
	v_fma_f32 v255, 2.0, v250, v253
	v_sub_f32_e32 v247, v247, v245
	v_sub_f32_e32 v253, v253, v251
	v_fma_f32 v246, -2.0, v244, v246
	v_fma_f32 v252, -2.0, v250, v252
	v_mul_f32_e32 v247, v247, v248
	v_mul_f32_e32 v253, v253, v254
	v_rcp_f32_e32 v247, v247
	v_rcp_f32_e32 v253, v253
	v_mul_f32_e32 v249, v249, v246
	v_mul_f32_e32 v255, v255, v252
	v_fma_f32 v19, v249, v247, v19
	v_fma_f32 v19, v255, v253, v19
	v_mul_f32_e32 v244, v86, v90
	v_mul_f32_e32 v250, v87, v91
	v_mul_f32_e64 v245, -v90, v90
	v_mul_f32_e64 v251, -v91, v91
	v_add_f32_e32 v246, v86, v90
	v_add_f32_e32 v252, v87, v91
	v_fma_f32 v245, -v86, v86, v245
	v_fma_f32 v251, -v87, v87, v251
	v_fma_f32 v247, v10, v246, v11
	v_fma_f32 v253, v10, v252, v11
	v_fma_f32 v246, v13, v98, v14
	v_fma_f32 v252, v13, v99, v14
	v_fma_f32 v248, v12, v94, v245
	v_fma_f32 v254, v12, v95, v251
	v_fma_f32 v249, 2.0, v244, v247
	v_fma_f32 v255, 2.0, v250, v253
	v_sub_f32_e32 v247, v247, v245
	v_sub_f32_e32 v253, v253, v251
	v_fma_f32 v246, -2.0, v244, v246
	v_fma_f32 v252, -2.0, v250, v252
	v_mul_f32_e32 v247, v247, v248
	v_mul_f32_e32 v253, v253, v254
	v_rcp_f32_e32 v247, v247
	v_rcp_f32_e32 v253, v253
	v_mul_f32_e32 v249, v249, v246
	v_mul_f32_e32 v255, v255, v252
	v_fma_f32 v20, v249, v247, v20
	v_fma_f32 v20, v255, v253, v20
	s_waitcnt lgkmcnt(0)
	v_mfma_f32_16x16x32_f16 v[84:87], v[28:31], v[228:231], 0
	v_mfma_f32_16x16x32_f16 v[88:91], v[28:31], v[232:235], 0
	v_mfma_f32_16x16x32_f16 v[92:95], v[28:31], v[236:239], v[0:3]
	v_mfma_f32_16x16x32_f16 v[96:99], v[28:31], v[240:243], 0
	v_mfma_f32_16x16x32_f16 v[84:87], v[32:35], v[36:39], v[84:87]
	v_mfma_f32_16x16x32_f16 v[88:91], v[32:35], v[44:47], v[88:91]
	v_mfma_f32_16x16x32_f16 v[92:95], v[32:35], v[52:55], v[92:95]
	v_mfma_f32_16x16x32_f16 v[96:99], v[32:35], v[60:63], v[96:99]
	v_mul_f32_e32 v244, v68, v72
	v_mul_f32_e32 v250, v69, v73
	v_mul_f32_e64 v245, -v72, v72
	v_mul_f32_e64 v251, -v73, v73
	v_add_f32_e32 v246, v68, v72
	v_add_f32_e32 v252, v69, v73
	v_fma_f32 v245, -v68, v68, v245
	v_fma_f32 v251, -v69, v69, v251
	v_fma_f32 v247, v10, v246, v11
	v_fma_f32 v253, v10, v252, v11
	v_fma_f32 v246, v13, v80, v14
	v_fma_f32 v252, v13, v81, v14
	v_fma_f32 v248, v12, v76, v245
	v_fma_f32 v254, v12, v77, v251
	v_fma_f32 v249, 2.0, v244, v247
	v_fma_f32 v255, 2.0, v250, v253
	v_sub_f32_e32 v247, v247, v245
	v_sub_f32_e32 v253, v253, v251
	v_fma_f32 v246, -2.0, v244, v246
	v_fma_f32 v252, -2.0, v250, v252
	v_mul_f32_e32 v247, v247, v248
	v_mul_f32_e32 v253, v253, v254
	v_rcp_f32_e32 v247, v247
	v_rcp_f32_e32 v253, v253
	v_mul_f32_e32 v249, v249, v246
	v_mul_f32_e32 v255, v255, v252
	v_fma_f32 v19, v249, v247, v19
	v_fma_f32 v19, v255, v253, v19
	v_mul_f32_e32 v244, v70, v74
	v_mul_f32_e32 v250, v71, v75
	v_mul_f32_e64 v245, -v74, v74
	v_mul_f32_e64 v251, -v75, v75
	v_add_f32_e32 v246, v70, v74
	v_add_f32_e32 v252, v71, v75
	v_fma_f32 v245, -v70, v70, v245
	v_fma_f32 v251, -v71, v71, v251
	v_fma_f32 v247, v10, v246, v11
	v_fma_f32 v253, v10, v252, v11
	v_fma_f32 v246, v13, v82, v14
	v_fma_f32 v252, v13, v83, v14
	v_fma_f32 v248, v12, v78, v245
	v_fma_f32 v254, v12, v79, v251
	v_fma_f32 v249, 2.0, v244, v247
	v_fma_f32 v255, 2.0, v250, v253
	v_sub_f32_e32 v247, v247, v245
	v_sub_f32_e32 v253, v253, v251
	v_fma_f32 v246, -2.0, v244, v246
	v_fma_f32 v252, -2.0, v250, v252
	v_mul_f32_e32 v247, v247, v248
	v_mul_f32_e32 v253, v253, v254
	v_rcp_f32_e32 v247, v247
	v_rcp_f32_e32 v253, v253
	v_mul_f32_e32 v249, v249, v246
	v_mul_f32_e32 v255, v255, v252
	v_fma_f32 v20, v249, v247, v20
	v_fma_f32 v20, v255, v253, v20
	v_mul_f32_e32 v244, v84, v88
	v_mul_f32_e32 v250, v85, v89
	v_mul_f32_e64 v245, -v88, v88
	v_mul_f32_e64 v251, -v89, v89
	v_add_f32_e32 v246, v84, v88
	v_add_f32_e32 v252, v85, v89
	v_fma_f32 v245, -v84, v84, v245
	v_fma_f32 v251, -v85, v85, v251
	v_fma_f32 v247, v10, v246, v11
	v_fma_f32 v253, v10, v252, v11
	v_fma_f32 v246, v13, v96, v14
	v_fma_f32 v252, v13, v97, v14
	v_fma_f32 v248, v12, v92, v245
	v_fma_f32 v254, v12, v93, v251
	v_fma_f32 v249, 2.0, v244, v247
	v_fma_f32 v255, 2.0, v250, v253
	v_sub_f32_e32 v247, v247, v245
	v_sub_f32_e32 v253, v253, v251
	v_fma_f32 v246, -2.0, v244, v246
	v_fma_f32 v252, -2.0, v250, v252
	v_mul_f32_e32 v247, v247, v248
	v_mul_f32_e32 v253, v253, v254
	v_rcp_f32_e32 v247, v247
	v_rcp_f32_e32 v253, v253
	v_mul_f32_e32 v249, v249, v246
	v_mul_f32_e32 v255, v255, v252
	v_mul_f32_e32 v249, v249, v247
	v_mul_f32_e32 v255, v255, v253
	v_fma_f32 v19, v249, v15, v19
	v_fma_f32 v19, v255, v16, v19
	v_mul_f32_e32 v244, v86, v90
	v_mul_f32_e32 v250, v87, v91
	v_mul_f32_e64 v245, -v90, v90
	v_mul_f32_e64 v251, -v91, v91
	v_add_f32_e32 v246, v86, v90
	v_add_f32_e32 v252, v87, v91
	v_fma_f32 v245, -v86, v86, v245
	v_fma_f32 v251, -v87, v87, v251
	v_fma_f32 v247, v10, v246, v11
	v_fma_f32 v253, v10, v252, v11
	v_fma_f32 v246, v13, v98, v14
	v_fma_f32 v252, v13, v99, v14
	v_fma_f32 v248, v12, v94, v245
	v_fma_f32 v254, v12, v95, v251
	v_fma_f32 v249, 2.0, v244, v247
	v_fma_f32 v255, 2.0, v250, v253
	v_sub_f32_e32 v247, v247, v245
	v_sub_f32_e32 v253, v253, v251
	v_fma_f32 v246, -2.0, v244, v246
	v_fma_f32 v252, -2.0, v250, v252
	v_mul_f32_e32 v247, v247, v248
	v_mul_f32_e32 v253, v253, v254
	v_rcp_f32_e32 v247, v247
	v_rcp_f32_e32 v253, v253
	v_mul_f32_e32 v249, v249, v246
	v_mul_f32_e32 v255, v255, v252
	v_mul_f32_e32 v249, v249, v247
	v_mul_f32_e32 v255, v255, v253
	v_fma_f32 v20, v249, v17, v20
	v_fma_f32 v20, v255, v18, v20
	s_waitcnt vmcnt(12)
	v_cvt_pk_f16_f32 v36, v100, v104
	v_cvt_pk_f16_f32 v52, v132, v136
	v_pk_add_f16 v36, v36, -0.5 op_sel_hi:[1,0]
	v_pk_add_f16 v52, v52, -0.5 op_sel_hi:[1,0]
	v_pk_mul_f16 v68, v52, v52
	v_pk_mul_f16 v84, v36, v52
	v_pk_fma_f16 v68, v36, v36, v68
	v_cvt_pk_f16_f32 v40, v101, v105
	v_cvt_pk_f16_f32 v56, v133, v137
	v_pk_add_f16 v40, v40, -0.5 op_sel_hi:[1,0]
	v_pk_add_f16 v56, v56, -0.5 op_sel_hi:[1,0]
	v_pk_mul_f16 v72, v56, v56
	v_pk_mul_f16 v88, v40, v56
	v_pk_fma_f16 v72, v40, v40, v72
	v_cvt_pk_f16_f32 v44, v102, v106
	v_cvt_pk_f16_f32 v60, v134, v138
	v_pk_add_f16 v44, v44, -0.5 op_sel_hi:[1,0]
	v_pk_add_f16 v60, v60, -0.5 op_sel_hi:[1,0]
	v_pk_mul_f16 v76, v60, v60
	v_pk_mul_f16 v92, v44, v60
	v_pk_fma_f16 v76, v44, v44, v76
	v_cvt_pk_f16_f32 v48, v103, v107
	v_cvt_pk_f16_f32 v64, v135, v139
	v_pk_add_f16 v48, v48, -0.5 op_sel_hi:[1,0]
	v_pk_add_f16 v64, v64, -0.5 op_sel_hi:[1,0]
	v_pk_mul_f16 v80, v64, v64
	v_pk_mul_f16 v96, v48, v64
	v_pk_fma_f16 v80, v48, v48, v80
	s_waitcnt vmcnt(8)
	v_cvt_pk_f16_f32 v37, v108, v112
	v_cvt_pk_f16_f32 v53, v140, v144
	v_pk_add_f16 v37, v37, -0.5 op_sel_hi:[1,0]
	v_pk_add_f16 v53, v53, -0.5 op_sel_hi:[1,0]
	v_pk_mul_f16 v69, v53, v53
	v_pk_mul_f16 v85, v37, v53
	v_pk_fma_f16 v69, v37, v37, v69
	v_cvt_pk_f16_f32 v41, v109, v113
	v_cvt_pk_f16_f32 v57, v141, v145
	v_pk_add_f16 v41, v41, -0.5 op_sel_hi:[1,0]
	v_pk_add_f16 v57, v57, -0.5 op_sel_hi:[1,0]
	v_pk_mul_f16 v73, v57, v57
	v_pk_mul_f16 v89, v41, v57
	v_pk_fma_f16 v73, v41, v41, v73
	v_cvt_pk_f16_f32 v45, v110, v114
	v_cvt_pk_f16_f32 v61, v142, v146
	v_pk_add_f16 v45, v45, -0.5 op_sel_hi:[1,0]
	v_pk_add_f16 v61, v61, -0.5 op_sel_hi:[1,0]
	v_pk_mul_f16 v77, v61, v61
	v_pk_mul_f16 v93, v45, v61
	v_pk_fma_f16 v77, v45, v45, v77
	v_cvt_pk_f16_f32 v49, v111, v115
	v_cvt_pk_f16_f32 v65, v143, v147
	v_pk_add_f16 v49, v49, -0.5 op_sel_hi:[1,0]
	v_pk_add_f16 v65, v65, -0.5 op_sel_hi:[1,0]
	v_pk_mul_f16 v81, v65, v65
	v_pk_mul_f16 v97, v49, v65
	v_pk_fma_f16 v81, v49, v49, v81
	s_waitcnt vmcnt(4)
	v_cvt_pk_f16_f32 v38, v116, v120
	v_cvt_pk_f16_f32 v54, v148, v152
	v_pk_add_f16 v38, v38, -0.5 op_sel_hi:[1,0]
	v_pk_add_f16 v54, v54, -0.5 op_sel_hi:[1,0]
	v_pk_mul_f16 v70, v54, v54
	v_pk_mul_f16 v86, v38, v54
	v_pk_fma_f16 v70, v38, v38, v70
	v_cvt_pk_f16_f32 v42, v117, v121
	v_cvt_pk_f16_f32 v58, v149, v153
	v_pk_add_f16 v42, v42, -0.5 op_sel_hi:[1,0]
	v_pk_add_f16 v58, v58, -0.5 op_sel_hi:[1,0]
	v_pk_mul_f16 v74, v58, v58
	v_pk_mul_f16 v90, v42, v58
	v_pk_fma_f16 v74, v42, v42, v74
	v_cvt_pk_f16_f32 v46, v118, v122
	v_cvt_pk_f16_f32 v62, v150, v154
	v_pk_add_f16 v46, v46, -0.5 op_sel_hi:[1,0]
	v_pk_add_f16 v62, v62, -0.5 op_sel_hi:[1,0]
	v_pk_mul_f16 v78, v62, v62
	v_pk_mul_f16 v94, v46, v62
	v_pk_fma_f16 v78, v46, v46, v78
	v_cvt_pk_f16_f32 v50, v119, v123
	v_cvt_pk_f16_f32 v66, v151, v155
	v_pk_add_f16 v50, v50, -0.5 op_sel_hi:[1,0]
	v_pk_add_f16 v66, v66, -0.5 op_sel_hi:[1,0]
	v_pk_mul_f16 v82, v66, v66
	v_pk_mul_f16 v98, v50, v66
	v_pk_fma_f16 v82, v50, v50, v82
	s_waitcnt vmcnt(0)
	v_cvt_pk_f16_f32 v39, v124, v128
	v_cvt_pk_f16_f32 v55, v156, v160
	v_pk_add_f16 v39, v39, -0.5 op_sel_hi:[1,0]
	v_pk_add_f16 v55, v55, -0.5 op_sel_hi:[1,0]
	v_pk_mul_f16 v71, v55, v55
	v_pk_mul_f16 v87, v39, v55
	v_pk_fma_f16 v71, v39, v39, v71
	v_cvt_pk_f16_f32 v43, v125, v129
	v_cvt_pk_f16_f32 v59, v157, v161
	v_pk_add_f16 v43, v43, -0.5 op_sel_hi:[1,0]
	v_pk_add_f16 v59, v59, -0.5 op_sel_hi:[1,0]
	v_pk_mul_f16 v75, v59, v59
	v_pk_mul_f16 v91, v43, v59
	v_pk_fma_f16 v75, v43, v43, v75
	v_cvt_pk_f16_f32 v47, v126, v130
	v_cvt_pk_f16_f32 v63, v158, v162
	v_pk_add_f16 v47, v47, -0.5 op_sel_hi:[1,0]
	v_pk_add_f16 v63, v63, -0.5 op_sel_hi:[1,0]
	v_pk_mul_f16 v79, v63, v63
	v_pk_mul_f16 v95, v47, v63
	v_pk_fma_f16 v79, v47, v47, v79
	v_cvt_pk_f16_f32 v51, v127, v131
	v_cvt_pk_f16_f32 v67, v159, v163
	v_pk_add_f16 v51, v51, -0.5 op_sel_hi:[1,0]
	v_pk_add_f16 v67, v67, -0.5 op_sel_hi:[1,0]
	v_pk_mul_f16 v83, v67, v67
	v_pk_mul_f16 v99, v51, v67
	v_pk_fma_f16 v83, v51, v51, v83
	v_mfma_f32_16x16x32_f16 v[132:135], v[164:167], v[28:31], 0
	v_mfma_f32_16x16x32_f16 v[136:139], v[168:171], v[28:31], 0
	v_mfma_f32_16x16x32_f16 v[140:143], v[172:175], v[28:31], 0
	v_mfma_f32_16x16x32_f16 v[144:147], v[176:179], v[28:31], 0
	v_mfma_f32_16x16x32_f16 v[132:135], v[36:39], v[32:35], v[132:135]
	v_mfma_f32_16x16x32_f16 v[136:139], v[40:43], v[32:35], v[136:139]
	v_mfma_f32_16x16x32_f16 v[140:143], v[44:47], v[32:35], v[140:143]
	v_mfma_f32_16x16x32_f16 v[144:147], v[48:51], v[32:35], v[144:147]
	v_mfma_f32_16x16x32_f16 v[148:151], v[180:183], v[28:31], 0
	v_mfma_f32_16x16x32_f16 v[152:155], v[184:187], v[28:31], 0
	v_mfma_f32_16x16x32_f16 v[156:159], v[188:191], v[28:31], 0
	v_mfma_f32_16x16x32_f16 v[160:163], v[192:195], v[28:31], 0
	v_mfma_f32_16x16x32_f16 v[148:151], v[52:55], v[32:35], v[148:151]
	v_mfma_f32_16x16x32_f16 v[152:155], v[56:59], v[32:35], v[152:155]
	v_mfma_f32_16x16x32_f16 v[156:159], v[60:63], v[32:35], v[156:159]
	v_mfma_f32_16x16x32_f16 v[160:163], v[64:67], v[32:35], v[160:163]
	v_cvt_pk_f16_f32 v100, v132, v136
	v_cvt_pk_f16_f32 v101, v140, v144
	v_cvt_pk_f16_f32 v102, v133, v137
	v_cvt_pk_f16_f32 v103, v141, v145
	v_cvt_pk_f16_f32 v104, v134, v138
	v_cvt_pk_f16_f32 v105, v142, v146
	v_cvt_pk_f16_f32 v106, v135, v139
	v_cvt_pk_f16_f32 v107, v143, v147
	v_mfma_f32_16x16x32_f16 v[132:135], v[196:199], v[28:31], 0
	v_mfma_f32_16x16x32_f16 v[136:139], v[200:203], v[28:31], 0
	v_mfma_f32_16x16x32_f16 v[140:143], v[204:207], v[28:31], 0
	v_mfma_f32_16x16x32_f16 v[144:147], v[208:211], v[28:31], 0
	v_mfma_f32_16x16x32_f16 v[132:135], v[68:71], v[32:35], v[132:135]
	v_mfma_f32_16x16x32_f16 v[136:139], v[72:75], v[32:35], v[136:139]
	v_mfma_f32_16x16x32_f16 v[140:143], v[76:79], v[32:35], v[140:143]
	v_mfma_f32_16x16x32_f16 v[144:147], v[80:83], v[32:35], v[144:147]
	v_cvt_pk_f16_f32 v108, v148, v152
	v_cvt_pk_f16_f32 v109, v156, v160
	v_cvt_pk_f16_f32 v110, v149, v153
	v_cvt_pk_f16_f32 v111, v157, v161
	v_cvt_pk_f16_f32 v112, v150, v154
	v_cvt_pk_f16_f32 v113, v158, v162
	v_cvt_pk_f16_f32 v114, v151, v155
	v_cvt_pk_f16_f32 v115, v159, v163
	v_mfma_f32_16x16x32_f16 v[148:151], v[212:215], v[28:31], 0
	v_mfma_f32_16x16x32_f16 v[152:155], v[216:219], v[28:31], 0
	v_mfma_f32_16x16x32_f16 v[156:159], v[220:223], v[28:31], 0
	v_mfma_f32_16x16x32_f16 v[160:163], v[224:227], v[28:31], 0
	v_mfma_f32_16x16x32_f16 v[148:151], v[84:87], v[32:35], v[148:151]
	v_mfma_f32_16x16x32_f16 v[152:155], v[88:91], v[32:35], v[152:155]
	v_mfma_f32_16x16x32_f16 v[156:159], v[92:95], v[32:35], v[156:159]
	v_mfma_f32_16x16x32_f16 v[160:163], v[96:99], v[32:35], v[160:163]
	v_cvt_pk_f16_f32 v116, v132, v136
	v_cvt_pk_f16_f32 v117, v140, v144
	v_cvt_pk_f16_f32 v118, v133, v137
	v_cvt_pk_f16_f32 v119, v141, v145
	v_cvt_pk_f16_f32 v120, v134, v138
	v_cvt_pk_f16_f32 v121, v142, v146
	v_cvt_pk_f16_f32 v122, v135, v139
	v_cvt_pk_f16_f32 v123, v143, v147
	v_cvt_pk_f16_f32 v124, v148, v152
	v_cvt_pk_f16_f32 v125, v156, v160
	v_cvt_pk_f16_f32 v126, v149, v153
	v_cvt_pk_f16_f32 v127, v157, v161
	v_cvt_pk_f16_f32 v128, v150, v154
	v_cvt_pk_f16_f32 v129, v158, v162
	v_cvt_pk_f16_f32 v130, v151, v155
	v_cvt_pk_f16_f32 v131, v159, v163
	v_and_b32_e32 v9, 0xffff9fff, v23
	v_cmp_gt_u32_e32 vcc, 48, v8
	s_nop 1
	v_cndmask_b32_e32 v9, v9, v23, vcc
	v_and_b32_e32 v244, 0xffffbfff, v23
	global_load_dwordx4 v[164:167], v9, s[84:85] offset:0 sc1 nt
	global_load_dwordx4 v[168:171], v9, s[84:85] offset:2048 sc1 nt
	global_load_dwordx4 v[180:183], v9, s[88:89] offset:0 sc1 nt
	global_load_dwordx4 v[184:187], v9, s[88:89] offset:2048 sc1 nt
	global_load_dwordx4 v[172:175], v244, s[86:87] offset:0 sc1 nt
	global_load_dwordx4 v[176:179], v244, s[86:87] offset:2048 sc1 nt
	global_load_dwordx4 v[188:191], v244, s[90:91] offset:0 sc1 nt
	global_load_dwordx4 v[192:195], v244, s[90:91] offset:2048 sc1 nt
	s_mov_b64 exec, s[38:39]
	ds_write_b128 v4, v[104:107] offset:16384
	ds_write_b128 v4, v[112:115] offset:16896
	ds_write_b128 v4, v[120:123] offset:17408
	ds_write_b128 v4, v[128:131] offset:17920
	s_mov_b64 exec, -1
	v_mfma_f32_16x16x32_f16 v[132:135], v[24:27], v[100:103], 0
	v_mfma_f32_16x16x32_f16 v[136:139], v[24:27], v[108:111], 0
	v_mfma_f32_16x16x32_f16 v[140:143], v[24:27], v[116:119], v[0:3]
	v_mfma_f32_16x16x32_f16 v[144:147], v[24:27], v[124:127], 0
	v_mfma_f32_16x16x32_f16 v[148:151], v[28:31], v[100:103], 0
	v_mfma_f32_16x16x32_f16 v[152:155], v[28:31], v[108:111], 0
	v_mfma_f32_16x16x32_f16 v[156:159], v[28:31], v[116:119], v[0:3]
	v_mfma_f32_16x16x32_f16 v[160:163], v[28:31], v[124:127], 0
	v_mfma_f32_16x16x32_f16 v[148:151], v[32:35], v[104:107], v[148:151]
	v_mfma_f32_16x16x32_f16 v[152:155], v[32:35], v[112:115], v[152:155]
	v_mfma_f32_16x16x32_f16 v[156:159], v[32:35], v[120:123], v[156:159]
	v_mfma_f32_16x16x32_f16 v[160:163], v[32:35], v[128:131], v[160:163]
	s_waitcnt lgkmcnt(0)
	ds_write_b32 v6, v6 offset:32
	ds_read_b32 v9, v7 offset:32
	v_mul_f32_e32 v244, v132, v136
	v_mul_f32_e32 v250, v133, v137
	v_mul_f32_e64 v245, -v136, v136
	v_mul_f32_e64 v251, -v137, v137
	v_add_f32_e32 v246, v132, v136
	v_add_f32_e32 v252, v133, v137
	v_fma_f32 v245, -v132, v132, v245
	v_fma_f32 v251, -v133, v133, v251
	v_fma_f32 v247, v10, v246, v11
	v_fma_f32 v253, v10, v252, v11
	v_fma_f32 v246, v13, v144, v14
	v_fma_f32 v252, v13, v145, v14
	v_fma_f32 v248, v12, v140, v245
	v_fma_f32 v254, v12, v141, v251
	v_fma_f32 v249, 2.0, v244, v247
	v_fma_f32 v255, 2.0, v250, v253
	v_sub_f32_e32 v247, v247, v245
	v_sub_f32_e32 v253, v253, v251
	v_fma_f32 v246, -2.0, v244, v246
	v_fma_f32 v252, -2.0, v250, v252
	v_mul_f32_e32 v247, v247, v248
	v_mul_f32_e32 v253, v253, v254
	v_rcp_f32_e32 v247, v247
	v_rcp_f32_e32 v253, v253
	v_mul_f32_e32 v249, v249, v246
	v_mul_f32_e32 v255, v255, v252
	v_fma_f32 v19, v249, v247, v19
	v_fma_f32 v19, v255, v253, v19
	v_mul_f32_e32 v244, v134, v138
	v_mul_f32_e32 v250, v135, v139
	v_mul_f32_e64 v245, -v138, v138
	v_mul_f32_e64 v251, -v139, v139
	v_add_f32_e32 v246, v134, v138
	v_add_f32_e32 v252, v135, v139
	v_fma_f32 v245, -v134, v134, v245
	v_fma_f32 v251, -v135, v135, v251
	v_fma_f32 v247, v10, v246, v11
	v_fma_f32 v253, v10, v252, v11
	v_fma_f32 v246, v13, v146, v14
	v_fma_f32 v252, v13, v147, v14
	v_fma_f32 v248, v12, v142, v245
	v_fma_f32 v254, v12, v143, v251
	v_fma_f32 v249, 2.0, v244, v247
	v_fma_f32 v255, 2.0, v250, v253
	v_sub_f32_e32 v247, v247, v245
	v_sub_f32_e32 v253, v253, v251
	v_fma_f32 v246, -2.0, v244, v246
	v_fma_f32 v252, -2.0, v250, v252
	v_mul_f32_e32 v247, v247, v248
	v_mul_f32_e32 v253, v253, v254
	v_rcp_f32_e32 v247, v247
	v_rcp_f32_e32 v253, v253
	v_mul_f32_e32 v249, v249, v246
	v_mul_f32_e32 v255, v255, v252
	v_fma_f32 v20, v249, v247, v20
	v_fma_f32 v20, v255, v253, v20
	v_mfma_f32_16x16x32_f16 v[132:135], v[24:27], v[104:107], 0
	v_mfma_f32_16x16x32_f16 v[136:139], v[24:27], v[112:115], 0
	v_mfma_f32_16x16x32_f16 v[140:143], v[24:27], v[120:123], v[0:3]
	v_mfma_f32_16x16x32_f16 v[144:147], v[24:27], v[128:131], 0
	s_waitcnt lgkmcnt(0)
	v_cmp_ne_u32_e32 vcc, 0, v9
	s_cbranch_vccnz .Lq_go_1
